# v15: + half-cost MoE tiles skip the LDS reads of the unused lower A half (P7, P8) (m1)
# speedup vs baseline: 1.0055x; 1.0055x over previous
.Lp7vg_mmjoin_a:
	s_barrier
	s_add_u32 s2, s44, 0x1000
	s_addc_u32 s3, s45, 0
	s_andn2_b64 vcc, exec, s[40:41]
	s_cbranch_vccnz .Lhalfskip_p7a
	ds_read_b128 v[58:61], v236 offset:16384
	ds_read_b128 v[62:65], v236 offset:17408
	ds_read_b128 v[50:53], v236 offset:18432
	ds_read_b128 v[54:57], v236 offset:19456
	ds_read_b128 v[42:45], v236 offset:20480
	ds_read_b128 v[46:49], v236 offset:21504
	ds_read_b128 v[34:37], v236 offset:22528
	ds_read_b128 v[38:41], v236 offset:23552
.Lhalfskip_p7a:
	s_cmp_eq_u32 s100, 3
	s_cbranch_scc1 .Lp7dma_w5_a
	s_waitcnt vmcnt(2)
	s_branch .Lp7dma_wd_a

.Lp7vg_mmjoin_b:
	s_barrier
	s_and_b64 vcc, exec, s[2:3]
	s_cbranch_vccnz .Lhalfskip_p7b
	ds_read_b128 v[58:61], v236 offset:49152
	ds_read_b128 v[62:65], v236 offset:50176
	ds_read_b128 v[50:53], v236 offset:51200
	ds_read_b128 v[54:57], v236 offset:52224
	ds_read_b128 v[42:45], v236 offset:53248
	ds_read_b128 v[46:49], v236 offset:54272
	ds_read_b128 v[34:37], v236 offset:55296
	ds_read_b128 v[38:41], v236 offset:56320

.LBB0_901:
	ds_read_b64_tr_b16 v[26:27], v207 offset:0
	ds_read_b64_tr_b16 v[28:29], v207 offset:1024
	ds_read_b64_tr_b16 v[30:31], v207 offset:8192
	ds_read_b64_tr_b16 v[32:33], v207 offset:9216
	ds_read_b64_tr_b16 v[18:19], v217 offset:0
	ds_read_b64_tr_b16 v[20:21], v217 offset:1024
	ds_read_b64_tr_b16 v[22:23], v217 offset:8192
	ds_read_b64_tr_b16 v[24:25], v217 offset:9216
	ds_read_b64_tr_b16 v[10:11], v214 offset:0
	ds_read_b64_tr_b16 v[12:13], v214 offset:1024
	ds_read_b64_tr_b16 v[14:15], v214 offset:8192
	ds_read_b64_tr_b16 v[16:17], v214 offset:9216
	ds_read_b64_tr_b16 v[2:3], v218 offset:0
	ds_read_b64_tr_b16 v[4:5], v218 offset:1024
	ds_read_b64_tr_b16 v[6:7], v218 offset:8192
	ds_read_b64_tr_b16 v[8:9], v218 offset:9216
	s_add_u32 s2, s50, 0xfffc0080
	s_addc_u32 s3, s51, -1
	s_cmp_eq_u32 s72, 12
	s_cselect_b32 s55, s29, s3
	s_cselect_b32 s54, s31, s2
	s_cselect_b32 s53, s35, s71
	s_cselect_b32 s52, s43, s70
	ds_read_b128 v[34:37], v223
	ds_read_b128 v[38:41], v223 offset:1024
	ds_read_b128 v[42:45], v223 offset:2048
	ds_read_b128 v[46:49], v223 offset:3072
	ds_read_b128 v[50:53], v223 offset:4096
	ds_read_b128 v[54:57], v223 offset:5120
	ds_read_b128 v[58:61], v223 offset:6144
	ds_read_b128 v[62:65], v223 offset:7168
	s_waitcnt vmcnt(6)
	s_waitcnt lgkmcnt(0)
	s_barrier
	s_setprio 1
	s_waitcnt lgkmcnt(0)
	v_mfma_scale_f32_16x16x128_f8f6f4 v[194:197], v[26:33], v[34:41], v[194:197], v1, v1 op_sel_hi:[0,0,0]
	v_mfma_scale_f32_16x16x128_f8f6f4 v[190:193], v[18:25], v[34:41], v[190:193], v1, v1 op_sel_hi:[0,0,0]
	v_mfma_scale_f32_16x16x128_f8f6f4 v[186:189], v[26:33], v[42:49], v[186:189], v1, v1 op_sel_hi:[0,0,0]
	v_mfma_scale_f32_16x16x128_f8f6f4 v[182:185], v[18:25], v[42:49], v[182:185], v1, v1 op_sel_hi:[0,0,0]
	v_lshl_add_u64 v[68:69], s[50:51], 0, v[208:209]
	s_add_i32 m0, s17, 0xc000
	s_nop 0
	global_load_lds_dwordx4 v[68:69], off
	v_mfma_scale_f32_16x16x128_f8f6f4 v[162:165], v[26:33], v[50:57], v[162:165], v1, v1 op_sel_hi:[0,0,0]
	v_mfma_scale_f32_16x16x128_f8f6f4 v[158:161], v[18:25], v[50:57], v[158:161], v1, v1 op_sel_hi:[0,0,0]
	v_mfma_scale_f32_16x16x128_f8f6f4 v[146:149], v[26:33], v[58:65], v[146:149], v1, v1 op_sel_hi:[0,0,0]
	v_mfma_scale_f32_16x16x128_f8f6f4 v[142:145], v[18:25], v[58:65], v[142:145], v1, v1 op_sel_hi:[0,0,0]
	s_setprio 0
	s_setprio 1
	v_mfma_scale_f32_16x16x128_f8f6f4 v[178:181], v[10:17], v[34:41], v[178:181], v1, v1 op_sel_hi:[0,0,0]
	v_mfma_scale_f32_16x16x128_f8f6f4 v[174:177], v[2:9], v[34:41], v[174:177], v1, v1 op_sel_hi:[0,0,0]
	v_lshl_add_u64 v[68:69], s[50:51], 0, v[210:211]
	s_add_i32 m0, s17, 0xe000
	s_nop 0
	global_load_lds_dwordx4 v[68:69], off
	v_mfma_scale_f32_16x16x128_f8f6f4 v[170:173], v[10:17], v[42:49], v[170:173], v1, v1 op_sel_hi:[0,0,0]
	v_mfma_scale_f32_16x16x128_f8f6f4 v[166:169], v[2:9], v[42:49], v[166:169], v1, v1 op_sel_hi:[0,0,0]
	v_mfma_scale_f32_16x16x128_f8f6f4 v[154:157], v[10:17], v[50:57], v[154:157], v1, v1 op_sel_hi:[0,0,0]
	v_mfma_scale_f32_16x16x128_f8f6f4 v[150:153], v[2:9], v[50:57], v[150:153], v1, v1 op_sel_hi:[0,0,0]
	v_mfma_scale_f32_16x16x128_f8f6f4 v[138:141], v[10:17], v[58:65], v[138:141], v1, v1 op_sel_hi:[0,0,0]
	v_mfma_scale_f32_16x16x128_f8f6f4 v[134:137], v[2:9], v[58:65], v[134:137], v1, v1 op_sel_hi:[0,0,0]
	s_setprio 0
	s_barrier
	s_andn2_b64 vcc, exec, s[48:49]
	s_cbranch_vccnz .Lhalfskip_p8a
	ds_read_b128 v[58:61], v223 offset:16384
	ds_read_b128 v[62:65], v223 offset:17408
	ds_read_b128 v[50:53], v223 offset:18432
	ds_read_b128 v[54:57], v223 offset:19456
	ds_read_b128 v[42:45], v223 offset:20480
	ds_read_b128 v[46:49], v223 offset:21504
	ds_read_b128 v[34:37], v223 offset:22528
	ds_read_b128 v[38:41], v223 offset:23552
.Lhalfskip_p8a:
	v_cmp_ne_u32_e64 s[2:3], 1, v225
	s_waitcnt vmcnt(2)
	s_waitcnt lgkmcnt(0)
	s_barrier
	s_cbranch_vccnz .Lp8_skip_b
	s_setprio 1
	s_waitcnt lgkmcnt(0)
	v_mfma_scale_f32_16x16x128_f8f6f4 v[130:133], v[26:33], v[58:65], v[130:133], v1, v1 op_sel_hi:[0,0,0]
	v_mfma_scale_f32_16x16x128_f8f6f4 v[126:129], v[18:25], v[58:65], v[126:129], v1, v1 op_sel_hi:[0,0,0]
	s_mov_b32 m0, s19
	v_lshl_add_u64 v[68:69], s[52:53], 0, v[200:201]
	global_load_lds_dwordx4 v[68:69], off
	v_mfma_scale_f32_16x16x128_f8f6f4 v[114:117], v[26:33], v[50:57], v[114:117], v1, v1 op_sel_hi:[0,0,0]
	v_mfma_scale_f32_16x16x128_f8f6f4 v[110:113], v[18:25], v[50:57], v[110:113], v1, v1 op_sel_hi:[0,0,0]
	v_lshl_add_u64 v[212:213], s[52:53], 0, v[204:205]
	s_mov_b32 m0, s33
	v_lshl_add_u64 v[68:69], v[68:69], 0, s[4:5]
	global_load_lds_dwordx4 v[212:213], off
	v_mfma_scale_f32_16x16x128_f8f6f4 v[98:101], v[26:33], v[42:49], v[98:101], v1, v1 op_sel_hi:[0,0,0]
	v_mfma_scale_f32_16x16x128_f8f6f4 v[94:97], v[18:25], v[42:49], v[94:97], v1, v1 op_sel_hi:[0,0,0]
	s_mov_b32 m0, s45
	s_nop 0
	global_load_lds_dwordx4 v[68:69], off
	v_mfma_scale_f32_16x16x128_f8f6f4 v[82:85], v[26:33], v[34:41], v[82:85], v1, v1 op_sel_hi:[0,0,0]
	v_mfma_scale_f32_16x16x128_f8f6f4 v[78:81], v[18:25], v[34:41], v[78:81], v1, v1 op_sel_hi:[0,0,0]
	s_setprio 0
	s_setprio 1
	v_mfma_scale_f32_16x16x128_f8f6f4 v[122:125], v[10:17], v[58:65], v[122:125], v1, v1 op_sel_hi:[0,0,0]
	v_lshl_add_u64 v[68:69], v[212:213], 0, s[4:5]
	s_mov_b32 m0, s47
	v_lshl_add_u64 v[212:213], s[54:55], 0, v[202:203]
	global_load_lds_dwordx4 v[68:69], off
	v_mfma_scale_f32_16x16x128_f8f6f4 v[118:121], v[2:9], v[58:65], v[118:121], v1, v1 op_sel_hi:[0,0,0]
	v_mfma_scale_f32_16x16x128_f8f6f4 v[106:109], v[10:17], v[50:57], v[106:109], v1, v1 op_sel_hi:[0,0,0]
	v_lshl_add_u64 v[68:69], s[54:55], 0, v[198:199]
	s_mov_b32 m0, s17
	s_nop 0
	global_load_lds_dwordx4 v[68:69], off
	v_mfma_scale_f32_16x16x128_f8f6f4 v[102:105], v[2:9], v[50:57], v[102:105], v1, v1 op_sel_hi:[0,0,0]
	v_mfma_scale_f32_16x16x128_f8f6f4 v[90:93], v[10:17], v[42:49], v[90:93], v1, v1 op_sel_hi:[0,0,0]
	s_mov_b32 m0, s58
	s_nop 0
	global_load_lds_dwordx4 v[212:213], off
	v_mfma_scale_f32_16x16x128_f8f6f4 v[86:89], v[2:9], v[42:49], v[86:89], v1, v1 op_sel_hi:[0,0,0]
	v_mfma_scale_f32_16x16x128_f8f6f4 v[74:77], v[10:17], v[34:41], v[74:77], v1, v1 op_sel_hi:[0,0,0]
	v_mfma_scale_f32_16x16x128_f8f6f4 v[70:73], v[2:9], v[34:41], v[70:73], v1, v1 op_sel_hi:[0,0,0]
	s_setprio 0
.LBB0_903:
	s_add_u32 s56, s52, 0x40000
	s_addc_u32 s57, s53, 0
	s_barrier
	ds_read_b64_tr_b16 v[26:27], v215 offset:0
	ds_read_b64_tr_b16 v[28:29], v215 offset:1024
	ds_read_b64_tr_b16 v[30:31], v215 offset:8192
	ds_read_b64_tr_b16 v[32:33], v215 offset:9216
	ds_read_b64_tr_b16 v[18:19], v219 offset:0
	ds_read_b64_tr_b16 v[20:21], v219 offset:1024
	ds_read_b64_tr_b16 v[22:23], v219 offset:8192
	ds_read_b64_tr_b16 v[24:25], v219 offset:9216
	ds_read_b64_tr_b16 v[10:11], v216 offset:0
	ds_read_b64_tr_b16 v[12:13], v216 offset:1024
	ds_read_b64_tr_b16 v[14:15], v216 offset:8192
	ds_read_b64_tr_b16 v[16:17], v216 offset:9216
	ds_read_b64_tr_b16 v[2:3], v220 offset:0
	ds_read_b64_tr_b16 v[4:5], v220 offset:1024
	ds_read_b64_tr_b16 v[6:7], v220 offset:8192
	ds_read_b64_tr_b16 v[8:9], v220 offset:9216
	s_add_u32 s54, s54, 0x40000
	s_addc_u32 s55, s55, 0
	ds_read_b128 v[34:37], v223 offset:32768
	ds_read_b128 v[38:41], v223 offset:33792
	ds_read_b128 v[42:45], v223 offset:34816
	ds_read_b128 v[46:49], v223 offset:35840
	ds_read_b128 v[50:53], v223 offset:36864
	ds_read_b128 v[54:57], v223 offset:37888
	ds_read_b128 v[58:61], v223 offset:38912
	ds_read_b128 v[62:65], v223 offset:39936
	s_waitcnt vmcnt(6)
	s_waitcnt lgkmcnt(0)
	s_barrier
	s_setprio 1
	s_waitcnt lgkmcnt(0)
	v_mfma_scale_f32_16x16x128_f8f6f4 v[194:197], v[26:33], v[34:41], v[194:197], v1, v1 op_sel_hi:[0,0,0]
	v_mfma_scale_f32_16x16x128_f8f6f4 v[190:193], v[18:25], v[34:41], v[190:193], v1, v1 op_sel_hi:[0,0,0]
	v_mfma_scale_f32_16x16x128_f8f6f4 v[186:189], v[26:33], v[42:49], v[186:189], v1, v1 op_sel_hi:[0,0,0]
	v_mfma_scale_f32_16x16x128_f8f6f4 v[182:185], v[18:25], v[42:49], v[182:185], v1, v1 op_sel_hi:[0,0,0]
	s_mov_b32 m0, s59
	v_lshl_add_u64 v[226:227], s[54:55], 0, v[198:199]
	global_load_lds_dwordx4 v[226:227], off
	v_mfma_scale_f32_16x16x128_f8f6f4 v[162:165], v[26:33], v[50:57], v[162:165], v1, v1 op_sel_hi:[0,0,0]
	v_mfma_scale_f32_16x16x128_f8f6f4 v[158:161], v[18:25], v[50:57], v[158:161], v1, v1 op_sel_hi:[0,0,0]
	v_mfma_scale_f32_16x16x128_f8f6f4 v[146:149], v[26:33], v[58:65], v[146:149], v1, v1 op_sel_hi:[0,0,0]
	v_mfma_scale_f32_16x16x128_f8f6f4 v[142:145], v[18:25], v[58:65], v[142:145], v1, v1 op_sel_hi:[0,0,0]
	s_setprio 0
	s_setprio 1
	v_mfma_scale_f32_16x16x128_f8f6f4 v[178:181], v[10:17], v[34:41], v[178:181], v1, v1 op_sel_hi:[0,0,0]
	v_mfma_scale_f32_16x16x128_f8f6f4 v[174:177], v[2:9], v[34:41], v[174:177], v1, v1 op_sel_hi:[0,0,0]
	v_lshl_add_u64 v[226:227], s[54:55], 0, v[202:203]
	s_mov_b32 m0, s60
	s_nop 0
	global_load_lds_dwordx4 v[226:227], off
	v_mfma_scale_f32_16x16x128_f8f6f4 v[170:173], v[10:17], v[42:49], v[170:173], v1, v1 op_sel_hi:[0,0,0]
	v_mfma_scale_f32_16x16x128_f8f6f4 v[166:169], v[2:9], v[42:49], v[166:169], v1, v1 op_sel_hi:[0,0,0]
	v_mfma_scale_f32_16x16x128_f8f6f4 v[154:157], v[10:17], v[50:57], v[154:157], v1, v1 op_sel_hi:[0,0,0]
	v_mfma_scale_f32_16x16x128_f8f6f4 v[150:153], v[2:9], v[50:57], v[150:153], v1, v1 op_sel_hi:[0,0,0]
	v_mfma_scale_f32_16x16x128_f8f6f4 v[138:141], v[10:17], v[58:65], v[138:141], v1, v1 op_sel_hi:[0,0,0]
	v_mfma_scale_f32_16x16x128_f8f6f4 v[134:137], v[2:9], v[58:65], v[134:137], v1, v1 op_sel_hi:[0,0,0]
	s_setprio 0
	s_barrier
	s_and_b64 vcc, exec, s[2:3]
	s_cbranch_vccnz .Lhalfskip_p8b
	ds_read_b128 v[58:61], v223 offset:49152
	ds_read_b128 v[62:65], v223 offset:50176
	ds_read_b128 v[50:53], v223 offset:51200
	ds_read_b128 v[54:57], v223 offset:52224
	ds_read_b128 v[42:45], v223 offset:53248
	ds_read_b128 v[46:49], v223 offset:54272
	ds_read_b128 v[34:37], v223 offset:55296
	ds_read_b128 v[38:41], v223 offset:56320
.Lhalfskip_p8b:
	s_waitcnt vmcnt(2)
	s_waitcnt lgkmcnt(0)
	s_barrier
	s_cbranch_vccnz .Lp8_skip_d
	s_setprio 1
	s_waitcnt lgkmcnt(0)
	v_mfma_scale_f32_16x16x128_f8f6f4 v[130:133], v[26:33], v[58:65], v[130:133], v1, v1 op_sel_hi:[0,0,0]
	v_mfma_scale_f32_16x16x128_f8f6f4 v[126:129], v[18:25], v[58:65], v[126:129], v1, v1 op_sel_hi:[0,0,0]
	v_lshl_add_u64 v[226:227], s[56:57], 0, v[200:201]
	s_add_i32 m0, s17, 0x18000
	s_nop 0
	global_load_lds_dwordx4 v[226:227], off
	v_mfma_scale_f32_16x16x128_f8f6f4 v[114:117], v[26:33], v[50:57], v[114:117], v1, v1 op_sel_hi:[0,0,0]
	v_mfma_scale_f32_16x16x128_f8f6f4 v[110:113], v[18:25], v[50:57], v[110:113], v1, v1 op_sel_hi:[0,0,0]
	s_add_i32 m0, s17, 0x1a000
	v_lshl_add_u64 v[226:227], s[56:57], 0, v[204:205]
	global_load_lds_dwordx4 v[226:227], off
	v_mfma_scale_f32_16x16x128_f8f6f4 v[98:101], v[26:33], v[42:49], v[98:101], v1, v1 op_sel_hi:[0,0,0]
	v_mfma_scale_f32_16x16x128_f8f6f4 v[94:97], v[18:25], v[42:49], v[94:97], v1, v1 op_sel_hi:[0,0,0]
	s_add_u32 s52, s52, 0x40100
	s_addc_u32 s53, s53, 0
	v_lshl_add_u64 v[226:227], s[52:53], 0, v[200:201]
	s_add_i32 m0, s17, 0x1c000
	v_lshl_add_u64 v[68:69], v[68:69], 0, s[12:13]
	global_load_lds_dwordx4 v[226:227], off
	v_mfma_scale_f32_16x16x128_f8f6f4 v[82:85], v[26:33], v[34:41], v[82:85], v1, v1 op_sel_hi:[0,0,0]
	v_mfma_scale_f32_16x16x128_f8f6f4 v[78:81], v[18:25], v[34:41], v[78:81], v1, v1 op_sel_hi:[0,0,0]
	s_setprio 0
	s_setprio 1
	v_mfma_scale_f32_16x16x128_f8f6f4 v[122:125], v[10:17], v[58:65], v[122:125], v1, v1 op_sel_hi:[0,0,0]
	v_lshl_add_u64 v[226:227], s[52:53], 0, v[204:205]
	s_add_i32 m0, s17, 0x1e000
	s_nop 0
	global_load_lds_dwordx4 v[226:227], off
	v_mfma_scale_f32_16x16x128_f8f6f4 v[118:121], v[2:9], v[58:65], v[118:121], v1, v1 op_sel_hi:[0,0,0]
	v_mfma_scale_f32_16x16x128_f8f6f4 v[106:109], v[10:17], v[50:57], v[106:109], v1, v1 op_sel_hi:[0,0,0]
	s_mov_b32 m0, s62
	s_nop 0
	global_load_lds_dwordx4 v[68:69], off
	v_mfma_scale_f32_16x16x128_f8f6f4 v[102:105], v[2:9], v[50:57], v[102:105], v1, v1 op_sel_hi:[0,0,0]
	v_mfma_scale_f32_16x16x128_f8f6f4 v[90:93], v[10:17], v[42:49], v[90:93], v1, v1 op_sel_hi:[0,0,0]
	v_lshl_add_u64 v[68:69], v[212:213], 0, s[12:13]
	s_mov_b32 m0, s63
	s_nop 0
	global_load_lds_dwordx4 v[68:69], off
	v_mfma_scale_f32_16x16x128_f8f6f4 v[86:89], v[2:9], v[42:49], v[86:89], v1, v1 op_sel_hi:[0,0,0]
	v_mfma_scale_f32_16x16x128_f8f6f4 v[74:77], v[10:17], v[34:41], v[74:77], v1, v1 op_sel_hi:[0,0,0]
	v_mfma_scale_f32_16x16x128_f8f6f4 v[70:73], v[2:9], v[34:41], v[70:73], v1, v1 op_sel_hi:[0,0,0]
	s_setprio 0
	s_branch .LBB0_900
